# v56 + next-layer weight conversion stores non-temporal (do not displace the activations in L2)
# speedup vs baseline: 1.0133x; 1.0032x over previous
.LBB0_155:
	v_readlane_b32 s38, v253, 32
	s_andn2_b64 vcc, exec, s[48:49]
	s_lshl_b32 s52, s38, 14
	v_readlane_b32 s39, v253, 33
	s_cbranch_vccnz .LBB0_159
	s_and_b64 vcc, exec, s[36:37]
	s_cbranch_vccnz .LBB0_158
	v_lshrrev_b32_e32 v0, 3, v198
	v_and_b32_e32 v67, 7, v235
	v_lshlrev_b32_e32 v98, 4, v67
	v_mul_u32_u24_e32 v69, 0x84, v0
	v_add3_u32 v69, s52, v98, v69
	s_waitcnt vmcnt(7)
	v_pk_mul_f32 v[30:31], v[30:31], v[66:67] op_sel_hi:[1,0]
	ds_write2_b32 v69, v30, v31 offset1:1
	v_pk_mul_f32 v[30:31], v[32:33], v[66:67] op_sel_hi:[1,0]
	ds_write2_b32 v69, v30, v31 offset0:2 offset1:3
	v_add_u32_e32 v32, 0x420, v69
	s_waitcnt vmcnt(6)
	v_pk_mul_f32 v[30:31], v[38:39], v[68:69] op_sel_hi:[1,0]
	ds_write2_b32 v32, v30, v31 offset1:1
	v_add_u32_e32 v32, 0x428, v69
	v_pk_mul_f32 v[30:31], v[40:41], v[68:69] op_sel_hi:[1,0]
	ds_write2_b32 v32, v30, v31 offset1:1
	v_add_u32_e32 v32, 0x840, v69
	s_waitcnt vmcnt(5)
	v_pk_mul_f32 v[30:31], v[34:35], v[74:75] op_sel_hi:[1,0]
	ds_write2_b32 v32, v30, v31 offset1:1
	v_add_u32_e32 v32, 0x848, v69
	v_pk_mul_f32 v[30:31], v[36:37], v[74:75] op_sel_hi:[1,0]
	ds_write2_b32 v32, v30, v31 offset1:1
	v_add_u32_e32 v32, 0xc60, v69
	s_waitcnt vmcnt(4)
	v_pk_mul_f32 v[30:31], v[46:47], v[76:77] op_sel_hi:[1,0]
	ds_write2_b32 v32, v30, v31 offset1:1
	v_add_u32_e32 v32, 0xc68, v69
	v_pk_mul_f32 v[30:31], v[48:49], v[76:77] op_sel_hi:[1,0]
	ds_write2_b32 v32, v30, v31 offset1:1
	v_add_u32_e32 v32, 0x1080, v69
	s_waitcnt vmcnt(3)
	v_pk_mul_f32 v[30:31], v[42:43], v[82:83] op_sel_hi:[1,0]
	ds_write2_b32 v32, v30, v31 offset1:1
	v_add_u32_e32 v32, 0x1088, v69
	v_pk_mul_f32 v[30:31], v[44:45], v[82:83] op_sel_hi:[1,0]
	ds_write2_b32 v32, v30, v31 offset1:1
	v_add_u32_e32 v32, 0x14a0, v69
	s_waitcnt vmcnt(2)
	v_pk_mul_f32 v[30:31], v[54:55], v[84:85] op_sel_hi:[1,0]
	ds_write2_b32 v32, v30, v31 offset1:1
	v_add_u32_e32 v32, 0x14a8, v69
	v_pk_mul_f32 v[30:31], v[56:57], v[84:85] op_sel_hi:[1,0]
	ds_write2_b32 v32, v30, v31 offset1:1
	v_add_u32_e32 v32, 0x18c0, v69
	s_waitcnt vmcnt(1)
	v_pk_mul_f32 v[30:31], v[50:51], v[90:91] op_sel_hi:[1,0]
	ds_write2_b32 v32, v30, v31 offset1:1
	v_add_u32_e32 v32, 0x18c8, v69
	v_pk_mul_f32 v[30:31], v[52:53], v[90:91] op_sel_hi:[1,0]
	ds_write2_b32 v32, v30, v31 offset1:1
	v_add_u32_e32 v32, 0x1ce0, v69
	s_waitcnt vmcnt(0)
	v_pk_mul_f32 v[30:31], v[58:59], v[92:93] op_sel_hi:[1,0]
	ds_write2_b32 v32, v30, v31 offset1:1
	v_add_u32_e32 v32, 0x1ce8, v69
	v_pk_mul_f32 v[30:31], v[60:61], v[92:93] op_sel_hi:[1,0]
	ds_write2_b32 v32, v30, v31 offset1:1
	s_waitcnt lgkmcnt(0)
	v_mul_u32_u24_e32 v30, 0x420, v67
	v_lshlrev_b32_e32 v31, 2, v0
	v_add3_u32 v52, s52, v30, v31
	ds_read2_b32 v[34:35], v52 offset0:33 offset1:41
	ds_read2_b32 v[36:37], v52 offset1:8
	ds_read2_b32 v[38:39], v52 offset0:66 offset1:74
	ds_read2_b32 v[40:41], v52 offset0:99 offset1:107
	ds_read2_b32 v[42:43], v52 offset0:132 offset1:140
	ds_read2_b32 v[44:45], v52 offset0:165 offset1:173
	ds_read2_b32 v[46:47], v52 offset0:198 offset1:206
	ds_read2_b32 v[48:49], v52 offset0:231 offset1:239
	v_lshlrev_b32_e32 v0, 11, v0
	v_lshl_add_u64 v[50:51], s[16:17], 0, v[0:1]
	v_mov_b32_e32 v99, v1
	s_waitcnt lgkmcnt(6)
	v_cvt_pk_bf16_f32 v30, v36, v34
	s_waitcnt lgkmcnt(4)
	v_cvt_pk_bf16_f32 v31, v38, v40
	s_waitcnt lgkmcnt(2)
	v_cvt_pk_bf16_f32 v32, v42, v44
	s_waitcnt lgkmcnt(0)
	v_cvt_pk_bf16_f32 v33, v46, v48
	v_lshl_add_u64 v[50:51], v[50:51], 0, v[98:99]
	global_store_dwordx4 v[50:51], v[30:33], off sc1 nt
	v_or_b32_e32 v34, 0x4000, v0
	s_nop 0
	v_cvt_pk_bf16_f32 v30, v37, v35
	v_cvt_pk_bf16_f32 v31, v39, v41
	v_cvt_pk_bf16_f32 v32, v43, v45
	v_cvt_pk_bf16_f32 v33, v47, v49
	v_mov_b32_e32 v35, v1
	ds_read2_b32 v[36:37], v52 offset0:49 offset1:57
	ds_read2_b32 v[38:39], v52 offset0:16 offset1:24
	ds_read2_b32 v[40:41], v52 offset0:82 offset1:90
	ds_read2_b32 v[42:43], v52 offset0:115 offset1:123
	ds_read2_b32 v[44:45], v52 offset0:148 offset1:156
	ds_read2_b32 v[46:47], v52 offset0:181 offset1:189
	ds_read2_b32 v[48:49], v52 offset0:214 offset1:222
	ds_read2_b32 v[50:51], v52 offset0:247 offset1:255
	v_lshl_add_u64 v[34:35], s[16:17], 0, v[34:35]
	v_lshl_add_u64 v[34:35], v[34:35], 0, v[98:99]
	global_store_dwordx4 v[34:35], v[30:33], off sc1 nt
	v_or_b32_e32 v34, 0x8000, v0
	v_mov_b32_e32 v35, v1
	v_lshl_add_u64 v[34:35], s[16:17], 0, v[34:35]
	s_waitcnt lgkmcnt(6)
	v_cvt_pk_bf16_f32 v30, v38, v36
	s_waitcnt lgkmcnt(4)
	v_cvt_pk_bf16_f32 v31, v40, v42
	s_waitcnt lgkmcnt(2)
	v_cvt_pk_bf16_f32 v32, v44, v46
	s_waitcnt lgkmcnt(0)
	v_cvt_pk_bf16_f32 v33, v48, v50
	v_lshl_add_u64 v[34:35], v[34:35], 0, v[98:99]
	v_or_b32_e32 v0, 0xc000, v0
	global_store_dwordx4 v[34:35], v[30:33], off sc1 nt
	v_lshl_add_u64 v[34:35], s[16:17], 0, v[0:1]
	v_lshl_add_u64 v[34:35], v[34:35], 0, v[98:99]
	v_cvt_pk_bf16_f32 v30, v39, v37
	v_cvt_pk_bf16_f32 v31, v41, v43
	v_cvt_pk_bf16_f32 v32, v45, v47
	v_cvt_pk_bf16_f32 v33, v49, v51
	global_store_dwordx4 v[34:35], v[30:33], off sc1 nt
	s_waitcnt lgkmcnt(0)

.LBB0_174:
	s_andn2_b64 vcc, exec, s[38:39]
	s_cbranch_vccnz .LBB0_178
	s_cmp_eq_u32 s31, 0
	s_cbranch_scc1 .LBB0_177
	v_lshrrev_b32_e32 v0, 3, v198
	s_waitcnt vmcnt(7)
	v_and_b32_e32 v31, 7, v235
	v_lshlrev_b32_e32 v30, 4, v31
	v_mul_u32_u24_e32 v32, 0x84, v0
	v_add3_u32 v32, s52, v30, v32
	v_pk_mul_f32 v[2:3], v[2:3], v[70:71] op_sel_hi:[1,0]
	ds_write2_b32 v32, v2, v3 offset1:1
	v_pk_mul_f32 v[2:3], v[4:5], v[70:71] op_sel_hi:[1,0]
	ds_write2_b32 v32, v2, v3 offset0:2 offset1:3
	v_add_u32_e32 v4, 0x420, v32
	s_waitcnt vmcnt(6)
	v_pk_mul_f32 v[2:3], v[10:11], v[72:73] op_sel_hi:[1,0]
	ds_write2_b32 v4, v2, v3 offset1:1
	v_add_u32_e32 v4, 0x428, v32
	v_pk_mul_f32 v[2:3], v[12:13], v[72:73] op_sel_hi:[1,0]
	ds_write2_b32 v4, v2, v3 offset1:1
	v_add_u32_e32 v4, 0x840, v32
	s_waitcnt vmcnt(5)
	v_pk_mul_f32 v[2:3], v[6:7], v[78:79] op_sel_hi:[1,0]
	ds_write2_b32 v4, v2, v3 offset1:1
	v_add_u32_e32 v4, 0x848, v32
	v_pk_mul_f32 v[2:3], v[8:9], v[78:79] op_sel_hi:[1,0]
	ds_write2_b32 v4, v2, v3 offset1:1
	v_add_u32_e32 v4, 0xc60, v32
	s_waitcnt vmcnt(4)
	v_pk_mul_f32 v[2:3], v[18:19], v[80:81] op_sel_hi:[1,0]
	ds_write2_b32 v4, v2, v3 offset1:1
	v_add_u32_e32 v4, 0xc68, v32
	v_pk_mul_f32 v[2:3], v[20:21], v[80:81] op_sel_hi:[1,0]
	ds_write2_b32 v4, v2, v3 offset1:1
	v_add_u32_e32 v4, 0x1080, v32
	s_waitcnt vmcnt(3)
	v_pk_mul_f32 v[2:3], v[14:15], v[86:87] op_sel_hi:[1,0]
	ds_write2_b32 v4, v2, v3 offset1:1
	v_add_u32_e32 v4, 0x1088, v32
	v_pk_mul_f32 v[2:3], v[16:17], v[86:87] op_sel_hi:[1,0]
	ds_write2_b32 v4, v2, v3 offset1:1
	v_add_u32_e32 v4, 0x14a0, v32
	s_waitcnt vmcnt(2)
	v_pk_mul_f32 v[2:3], v[26:27], v[88:89] op_sel_hi:[1,0]
	ds_write2_b32 v4, v2, v3 offset1:1
	v_add_u32_e32 v4, 0x14a8, v32
	v_pk_mul_f32 v[2:3], v[28:29], v[88:89] op_sel_hi:[1,0]
	ds_write2_b32 v4, v2, v3 offset1:1
	v_add_u32_e32 v4, 0x18c0, v32
	s_waitcnt vmcnt(1)
	v_pk_mul_f32 v[2:3], v[22:23], v[94:95] op_sel_hi:[1,0]
	ds_write2_b32 v4, v2, v3 offset1:1
	v_add_u32_e32 v4, 0x18c8, v32
	v_pk_mul_f32 v[2:3], v[24:25], v[94:95] op_sel_hi:[1,0]
	ds_write2_b32 v4, v2, v3 offset1:1
	v_add_u32_e32 v4, 0x1ce0, v32
	s_waitcnt vmcnt(0)
	v_pk_mul_f32 v[2:3], v[62:63], v[96:97] op_sel_hi:[1,0]
	ds_write2_b32 v4, v2, v3 offset1:1
	v_add_u32_e32 v4, 0x1ce8, v32
	v_pk_mul_f32 v[2:3], v[64:65], v[96:97] op_sel_hi:[1,0]
	ds_write2_b32 v4, v2, v3 offset1:1
	s_waitcnt lgkmcnt(0)
	v_mul_u32_u24_e32 v2, 0x420, v31
	v_lshlrev_b32_e32 v3, 2, v0
	v_add3_u32 v24, s52, v2, v3
	ds_read2_b32 v[6:7], v24 offset0:33 offset1:41
	ds_read2_b32 v[8:9], v24 offset1:8
	ds_read2_b32 v[10:11], v24 offset0:66 offset1:74
	ds_read2_b32 v[12:13], v24 offset0:99 offset1:107
	ds_read2_b32 v[14:15], v24 offset0:132 offset1:140
	ds_read2_b32 v[16:17], v24 offset0:165 offset1:173
	ds_read2_b32 v[18:19], v24 offset0:198 offset1:206
	ds_read2_b32 v[20:21], v24 offset0:231 offset1:239
	v_lshlrev_b32_e32 v0, 11, v0
	v_lshl_add_u64 v[22:23], s[14:15], 0, v[0:1]
	v_mov_b32_e32 v31, v1
	s_waitcnt lgkmcnt(6)
	v_cvt_pk_bf16_f32 v2, v8, v6
	s_waitcnt lgkmcnt(4)
	v_cvt_pk_bf16_f32 v3, v10, v12
	s_waitcnt lgkmcnt(2)
	v_cvt_pk_bf16_f32 v4, v14, v16
	s_waitcnt lgkmcnt(0)
	v_cvt_pk_bf16_f32 v5, v18, v20
	v_lshl_add_u64 v[22:23], v[22:23], 0, v[30:31]
	global_store_dwordx4 v[22:23], v[2:5], off sc1 nt
	v_or_b32_e32 v6, 0x4000, v0
	s_nop 0
	v_cvt_pk_bf16_f32 v2, v9, v7
	v_cvt_pk_bf16_f32 v3, v11, v13
	v_cvt_pk_bf16_f32 v4, v15, v17
	v_cvt_pk_bf16_f32 v5, v19, v21
	v_mov_b32_e32 v7, v1
	ds_read2_b32 v[8:9], v24 offset0:49 offset1:57
	ds_read2_b32 v[10:11], v24 offset0:16 offset1:24
	ds_read2_b32 v[12:13], v24 offset0:82 offset1:90
	ds_read2_b32 v[14:15], v24 offset0:115 offset1:123
	ds_read2_b32 v[16:17], v24 offset0:148 offset1:156
	ds_read2_b32 v[18:19], v24 offset0:181 offset1:189
	ds_read2_b32 v[20:21], v24 offset0:214 offset1:222
	ds_read2_b32 v[22:23], v24 offset0:247 offset1:255
	v_lshl_add_u64 v[6:7], s[14:15], 0, v[6:7]
	v_lshl_add_u64 v[6:7], v[6:7], 0, v[30:31]
	global_store_dwordx4 v[6:7], v[2:5], off sc1 nt
	v_or_b32_e32 v6, 0x8000, v0
	v_mov_b32_e32 v7, v1
	v_lshl_add_u64 v[6:7], s[14:15], 0, v[6:7]
	s_waitcnt lgkmcnt(6)
	v_cvt_pk_bf16_f32 v2, v10, v8
	s_waitcnt lgkmcnt(4)
	v_cvt_pk_bf16_f32 v3, v12, v14
	s_waitcnt lgkmcnt(2)
	v_cvt_pk_bf16_f32 v4, v16, v18
	s_waitcnt lgkmcnt(0)
	v_cvt_pk_bf16_f32 v5, v20, v22
	v_lshl_add_u64 v[6:7], v[6:7], 0, v[30:31]
	v_or_b32_e32 v0, 0xc000, v0
	global_store_dwordx4 v[6:7], v[2:5], off sc1 nt
	v_lshl_add_u64 v[6:7], s[14:15], 0, v[0:1]
	v_lshl_add_u64 v[6:7], v[6:7], 0, v[30:31]
	v_cvt_pk_bf16_f32 v2, v11, v9
	v_cvt_pk_bf16_f32 v3, v13, v15
	v_cvt_pk_bf16_f32 v4, v17, v19
	v_cvt_pk_bf16_f32 v5, v21, v23
	global_store_dwordx4 v[6:7], v[2:5], off sc1 nt
	s_waitcnt lgkmcnt(0)

.LBB0_193:
	s_andn2_b64 vcc, exec, s[38:39]
	s_cbranch_vccnz .LBB0_197
	s_cmp_eq_u32 s31, 0
	s_cbranch_scc1 .LBB0_196
	v_lshrrev_b32_e32 v0, 3, v198
	s_waitcnt vmcnt(0)
	v_and_b32_e32 v63, 7, v235
	v_lshlrev_b32_e32 v62, 4, v63
	v_mul_u32_u24_e32 v64, 0x84, v0
	v_add3_u32 v64, s52, v62, v64
	v_pk_mul_f32 v[34:35], v[34:35], v[74:75] op_sel_hi:[1,0]
	ds_write2_b32 v64, v34, v35 offset1:1
	v_pk_mul_f32 v[34:35], v[36:37], v[74:75] op_sel_hi:[1,0]
	ds_write2_b32 v64, v34, v35 offset0:2 offset1:3
	v_add_u32_e32 v36, 0x420, v64
	v_pk_mul_f32 v[34:35], v[42:43], v[76:77] op_sel_hi:[1,0]
	ds_write2_b32 v36, v34, v35 offset1:1
	v_add_u32_e32 v36, 0x428, v64
	v_pk_mul_f32 v[34:35], v[44:45], v[76:77] op_sel_hi:[1,0]
	ds_write2_b32 v36, v34, v35 offset1:1
	v_add_u32_e32 v36, 0x840, v64
	v_pk_mul_f32 v[34:35], v[38:39], v[82:83] op_sel_hi:[1,0]
	ds_write2_b32 v36, v34, v35 offset1:1
	v_add_u32_e32 v36, 0x848, v64
	v_pk_mul_f32 v[34:35], v[40:41], v[82:83] op_sel_hi:[1,0]
	ds_write2_b32 v36, v34, v35 offset1:1
	v_add_u32_e32 v36, 0xc60, v64
	v_pk_mul_f32 v[34:35], v[50:51], v[84:85] op_sel_hi:[1,0]
	ds_write2_b32 v36, v34, v35 offset1:1
	v_add_u32_e32 v36, 0xc68, v64
	v_pk_mul_f32 v[34:35], v[52:53], v[84:85] op_sel_hi:[1,0]
	ds_write2_b32 v36, v34, v35 offset1:1
	v_add_u32_e32 v36, 0x1080, v64
	v_pk_mul_f32 v[34:35], v[46:47], v[90:91] op_sel_hi:[1,0]
	ds_write2_b32 v36, v34, v35 offset1:1
	v_add_u32_e32 v36, 0x1088, v64
	v_pk_mul_f32 v[34:35], v[48:49], v[90:91] op_sel_hi:[1,0]
	ds_write2_b32 v36, v34, v35 offset1:1
	v_add_u32_e32 v36, 0x14a0, v64
	v_pk_mul_f32 v[34:35], v[58:59], v[92:93] op_sel_hi:[1,0]
	ds_write2_b32 v36, v34, v35 offset1:1
	v_add_u32_e32 v36, 0x14a8, v64
	v_pk_mul_f32 v[34:35], v[60:61], v[92:93] op_sel_hi:[1,0]
	ds_write2_b32 v36, v34, v35 offset1:1
	v_add_u32_e32 v36, 0x18c0, v64
	v_pk_mul_f32 v[34:35], v[54:55], v[98:99] op_sel_hi:[1,0]
	ds_write2_b32 v36, v34, v35 offset1:1
	v_add_u32_e32 v36, 0x18c8, v64
	v_pk_mul_f32 v[34:35], v[56:57], v[98:99] op_sel_hi:[1,0]
	ds_write2_b32 v36, v34, v35 offset1:1
	v_add_u32_e32 v36, 0x1ce0, v64
	v_pk_mul_f32 v[34:35], v[66:67], v[100:101] op_sel_hi:[1,0]
	ds_write2_b32 v36, v34, v35 offset1:1
	v_add_u32_e32 v36, 0x1ce8, v64
	v_pk_mul_f32 v[34:35], v[68:69], v[100:101] op_sel_hi:[1,0]
	ds_write2_b32 v36, v34, v35 offset1:1
	s_waitcnt lgkmcnt(0)
	v_mul_u32_u24_e32 v34, 0x420, v63
	v_lshlrev_b32_e32 v35, 2, v0
	v_add3_u32 v56, s52, v34, v35
	ds_read2_b32 v[38:39], v56 offset0:33 offset1:41
	ds_read2_b32 v[40:41], v56 offset1:8
	ds_read2_b32 v[42:43], v56 offset0:66 offset1:74
	ds_read2_b32 v[44:45], v56 offset0:99 offset1:107
	ds_read2_b32 v[46:47], v56 offset0:132 offset1:140
	ds_read2_b32 v[48:49], v56 offset0:165 offset1:173
	ds_read2_b32 v[50:51], v56 offset0:198 offset1:206
	ds_read2_b32 v[52:53], v56 offset0:231 offset1:239
	v_lshlrev_b32_e32 v0, 11, v0
	v_lshl_add_u64 v[54:55], s[16:17], 0, v[0:1]
	v_mov_b32_e32 v63, v1
	s_waitcnt lgkmcnt(6)
	v_cvt_pk_bf16_f32 v34, v40, v38
	s_waitcnt lgkmcnt(4)
	v_cvt_pk_bf16_f32 v35, v42, v44
	s_waitcnt lgkmcnt(2)
	v_cvt_pk_bf16_f32 v36, v46, v48
	s_waitcnt lgkmcnt(0)
	v_cvt_pk_bf16_f32 v37, v50, v52
	v_lshl_add_u64 v[54:55], v[54:55], 0, v[62:63]
	global_store_dwordx4 v[54:55], v[34:37], off sc1 nt
	v_or_b32_e32 v38, 0x4000, v0
	s_nop 0
	v_cvt_pk_bf16_f32 v34, v41, v39
	v_cvt_pk_bf16_f32 v35, v43, v45
	v_cvt_pk_bf16_f32 v36, v47, v49
	v_cvt_pk_bf16_f32 v37, v51, v53
	v_mov_b32_e32 v39, v1
	ds_read2_b32 v[40:41], v56 offset0:49 offset1:57
	ds_read2_b32 v[42:43], v56 offset0:16 offset1:24
	ds_read2_b32 v[44:45], v56 offset0:82 offset1:90
	ds_read2_b32 v[46:47], v56 offset0:115 offset1:123
	ds_read2_b32 v[48:49], v56 offset0:148 offset1:156
	ds_read2_b32 v[50:51], v56 offset0:181 offset1:189
	ds_read2_b32 v[52:53], v56 offset0:214 offset1:222
	ds_read2_b32 v[54:55], v56 offset0:247 offset1:255
	v_lshl_add_u64 v[38:39], s[16:17], 0, v[38:39]
	v_lshl_add_u64 v[38:39], v[38:39], 0, v[62:63]
	global_store_dwordx4 v[38:39], v[34:37], off sc1 nt
	v_or_b32_e32 v38, 0x8000, v0
	v_mov_b32_e32 v39, v1
	v_lshl_add_u64 v[38:39], s[16:17], 0, v[38:39]
	s_waitcnt lgkmcnt(6)
	v_cvt_pk_bf16_f32 v34, v42, v40
	s_waitcnt lgkmcnt(4)
	v_cvt_pk_bf16_f32 v35, v44, v46
	s_waitcnt lgkmcnt(2)
	v_cvt_pk_bf16_f32 v36, v48, v50
	s_waitcnt lgkmcnt(0)
	v_cvt_pk_bf16_f32 v37, v52, v54
	v_lshl_add_u64 v[38:39], v[38:39], 0, v[62:63]
	v_or_b32_e32 v0, 0xc000, v0
	global_store_dwordx4 v[38:39], v[34:37], off sc1 nt
	v_lshl_add_u64 v[38:39], s[16:17], 0, v[0:1]
	v_lshl_add_u64 v[38:39], v[38:39], 0, v[62:63]
	v_cvt_pk_bf16_f32 v34, v43, v41
	v_cvt_pk_bf16_f32 v35, v45, v47
	v_cvt_pk_bf16_f32 v36, v49, v51
	v_cvt_pk_bf16_f32 v37, v53, v55
	global_store_dwordx4 v[38:39], v[34:37], off sc1 nt
	s_waitcnt lgkmcnt(0)

.LBB0_215:
	s_andn2_b64 vcc, exec, s[50:51]
	s_cbranch_vccnz .LBB0_219
	s_cmp_eq_u32 s31, 0
	s_cbranch_scc1 .LBB0_218
	s_waitcnt vmcnt(6)
	v_pk_mul_f32 v[2:3], v[120:121], v[2:3] op_sel_hi:[0,1]
	ds_write2_b32 v101, v2, v3 offset1:1
	v_pk_mul_f32 v[2:3], v[120:121], v[4:5] op_sel_hi:[0,1]
	ds_write2_b32 v101, v2, v3 offset0:2 offset1:3
	s_waitcnt vmcnt(7)
	v_pk_mul_f32 v[2:3], v[118:119], v[10:11] op_sel_hi:[0,1]
	v_add_u32_e32 v0, 0x420, v101
	ds_write2_b32 v0, v2, v3 offset1:1
	v_pk_mul_f32 v[2:3], v[118:119], v[12:13] op_sel_hi:[0,1]
	v_add_u32_e32 v0, 0x428, v101
	ds_write2_b32 v0, v2, v3 offset1:1
	s_waitcnt vmcnt(6)
	v_pk_mul_f32 v[2:3], v[124:125], v[6:7] op_sel_hi:[0,1]
	v_add_u32_e32 v0, 0x840, v101
	ds_write2_b32 v0, v2, v3 offset1:1
	v_pk_mul_f32 v[2:3], v[124:125], v[8:9] op_sel_hi:[0,1]
	v_add_u32_e32 v0, 0x848, v101
	ds_write2_b32 v0, v2, v3 offset1:1
	s_waitcnt vmcnt(5)
	v_pk_mul_f32 v[2:3], v[122:123], v[22:23] op_sel_hi:[0,1]
	v_add_u32_e32 v0, 0xc60, v101
	ds_write2_b32 v0, v2, v3 offset1:1
	v_pk_mul_f32 v[2:3], v[122:123], v[24:25] op_sel_hi:[0,1]
	v_add_u32_e32 v0, 0xc68, v101
	ds_write2_b32 v0, v2, v3 offset1:1
	s_waitcnt vmcnt(4)
	v_pk_mul_f32 v[2:3], v[128:129], v[14:15] op_sel_hi:[0,1]
	v_add_u32_e32 v0, 0x1080, v101
	ds_write2_b32 v0, v2, v3 offset1:1
	v_pk_mul_f32 v[2:3], v[128:129], v[16:17] op_sel_hi:[0,1]
	v_add_u32_e32 v0, 0x1088, v101
	ds_write2_b32 v0, v2, v3 offset1:1
	s_waitcnt vmcnt(5)
	v_pk_mul_f32 v[2:3], v[126:127], v[26:27] op_sel_hi:[0,1]
	v_add_u32_e32 v0, 0x14a0, v101
	ds_write2_b32 v0, v2, v3 offset1:1
	v_pk_mul_f32 v[2:3], v[126:127], v[28:29] op_sel_hi:[0,1]
	v_add_u32_e32 v0, 0x14a8, v101
	ds_write2_b32 v0, v2, v3 offset1:1
	s_waitcnt vmcnt(4)
	v_pk_mul_f32 v[2:3], v[132:133], v[18:19] op_sel_hi:[0,1]
	v_add_u32_e32 v0, 0x18c0, v101
	ds_write2_b32 v0, v2, v3 offset1:1
	v_pk_mul_f32 v[2:3], v[132:133], v[20:21] op_sel_hi:[0,1]
	v_add_u32_e32 v0, 0x18c8, v101
	ds_write2_b32 v0, v2, v3 offset1:1
	s_waitcnt vmcnt(0)
	v_pk_mul_f32 v[2:3], v[130:131], v[30:31] op_sel_hi:[0,1]
	v_add_u32_e32 v0, 0x1ce0, v101
	ds_write2_b32 v0, v2, v3 offset1:1
	v_pk_mul_f32 v[2:3], v[130:131], v[32:33] op_sel_hi:[0,1]
	v_add_u32_e32 v0, 0x1ce8, v101
	ds_write2_b32 v0, v2, v3 offset1:1
	s_waitcnt lgkmcnt(0)
	ds_read2_b32 v[6:7], v99 offset0:33 offset1:41
	ds_read2_b32 v[8:9], v99 offset1:8
	ds_read2_b32 v[10:11], v99 offset0:66 offset1:74
	ds_read2_b32 v[12:13], v99 offset0:99 offset1:107
	ds_read2_b32 v[14:15], v99 offset0:132 offset1:140
	ds_read2_b32 v[16:17], v99 offset0:165 offset1:173
	ds_read2_b32 v[18:19], v99 offset0:198 offset1:206
	ds_read2_b32 v[20:21], v99 offset0:231 offset1:239
	v_lshl_add_u64 v[22:23], s[14:15], 0, v[116:117]
	v_lshlrev_b32_e32 v0, 1, v106
	s_waitcnt lgkmcnt(6)
	v_cvt_pk_bf16_f32 v2, v8, v6
	s_waitcnt lgkmcnt(4)
	v_cvt_pk_bf16_f32 v3, v10, v12
	s_waitcnt lgkmcnt(2)
	v_cvt_pk_bf16_f32 v4, v14, v16
	s_waitcnt lgkmcnt(0)
	v_cvt_pk_bf16_f32 v5, v18, v20
	v_lshl_add_u64 v[22:23], v[22:23], 0, v[0:1]
	global_store_dwordx4 v[22:23], v[2:5], off sc1 nt
	s_nop 1
	v_cvt_pk_bf16_f32 v2, v9, v7
	v_cvt_pk_bf16_f32 v3, v11, v13
	v_cvt_pk_bf16_f32 v4, v15, v17
	v_cvt_pk_bf16_f32 v5, v19, v21
	ds_read2_b32 v[8:9], v99 offset0:49 offset1:57
	ds_read2_b32 v[10:11], v99 offset0:16 offset1:24
	ds_read2_b32 v[12:13], v99 offset0:82 offset1:90
	ds_read2_b32 v[14:15], v99 offset0:115 offset1:123
	ds_read2_b32 v[16:17], v99 offset0:148 offset1:156
	ds_read2_b32 v[18:19], v99 offset0:181 offset1:189
	ds_read2_b32 v[20:21], v99 offset0:214 offset1:222
	ds_read2_b32 v[22:23], v99 offset0:247 offset1:255
	v_lshl_add_u64 v[6:7], s[14:15], 0, v[114:115]
	v_lshl_add_u64 v[6:7], v[6:7], 0, v[0:1]
	global_store_dwordx4 v[6:7], v[2:5], off sc1 nt
	v_lshl_add_u64 v[6:7], s[14:15], 0, v[112:113]
	v_lshl_add_u64 v[6:7], v[6:7], 0, v[0:1]
	s_waitcnt lgkmcnt(6)
	v_cvt_pk_bf16_f32 v2, v10, v8
	s_waitcnt lgkmcnt(4)
	v_cvt_pk_bf16_f32 v3, v12, v14
	s_waitcnt lgkmcnt(2)
	v_cvt_pk_bf16_f32 v4, v16, v18
	s_waitcnt lgkmcnt(0)
	v_cvt_pk_bf16_f32 v5, v20, v22
	global_store_dwordx4 v[6:7], v[2:5], off sc1 nt
	v_lshl_add_u64 v[6:7], s[14:15], 0, v[110:111]
	v_lshl_add_u64 v[6:7], v[6:7], 0, v[0:1]
	v_cvt_pk_bf16_f32 v2, v11, v9
	v_cvt_pk_bf16_f32 v3, v13, v15
	v_cvt_pk_bf16_f32 v4, v17, v19
	v_cvt_pk_bf16_f32 v5, v21, v23
	global_store_dwordx4 v[6:7], v[2:5], off sc1 nt
	s_waitcnt lgkmcnt(0)

.LBB0_233:
	s_andn2_b64 vcc, exec, s[50:51]
	s_cbranch_vccnz .LBB0_200
	s_cmp_eq_u32 s31, 0
	s_cbranch_scc1 .LBB0_199
	s_waitcnt vmcnt(6)
	v_pk_mul_f32 v[2:3], v[2:3], v[120:121] op_sel_hi:[1,0]
	ds_write2_b32 v101, v2, v3 offset1:1
	v_pk_mul_f32 v[2:3], v[4:5], v[120:121] op_sel_hi:[1,0]
	ds_write2_b32 v101, v2, v3 offset0:2 offset1:3
	v_pk_mul_f32 v[2:3], v[10:11], v[118:119] op_sel_hi:[1,0]
	v_add_u32_e32 v0, 0x420, v101
	ds_write2_b32 v0, v2, v3 offset1:1
	v_pk_mul_f32 v[2:3], v[12:13], v[118:119] op_sel_hi:[1,0]
	v_add_u32_e32 v0, 0x428, v101
	ds_write2_b32 v0, v2, v3 offset1:1
	v_pk_mul_f32 v[2:3], v[6:7], v[124:125] op_sel_hi:[1,0]
	v_add_u32_e32 v0, 0x840, v101
	ds_write2_b32 v0, v2, v3 offset1:1
	v_pk_mul_f32 v[2:3], v[8:9], v[124:125] op_sel_hi:[1,0]
	v_add_u32_e32 v0, 0x848, v101
	ds_write2_b32 v0, v2, v3 offset1:1
	s_waitcnt vmcnt(5)
	v_pk_mul_f32 v[2:3], v[22:23], v[122:123] op_sel_hi:[1,0]
	v_add_u32_e32 v0, 0xc60, v101
	ds_write2_b32 v0, v2, v3 offset1:1
	v_pk_mul_f32 v[2:3], v[24:25], v[122:123] op_sel_hi:[1,0]
	v_add_u32_e32 v0, 0xc68, v101
	ds_write2_b32 v0, v2, v3 offset1:1
	s_waitcnt vmcnt(4)
	v_pk_mul_f32 v[2:3], v[14:15], v[128:129] op_sel_hi:[1,0]
	v_add_u32_e32 v0, 0x1080, v101
	ds_write2_b32 v0, v2, v3 offset1:1
	v_pk_mul_f32 v[2:3], v[16:17], v[128:129] op_sel_hi:[1,0]
	v_add_u32_e32 v0, 0x1088, v101
	ds_write2_b32 v0, v2, v3 offset1:1
	v_pk_mul_f32 v[2:3], v[26:27], v[126:127] op_sel_hi:[1,0]
	v_add_u32_e32 v0, 0x14a0, v101
	ds_write2_b32 v0, v2, v3 offset1:1
	v_pk_mul_f32 v[2:3], v[28:29], v[126:127] op_sel_hi:[1,0]
	v_add_u32_e32 v0, 0x14a8, v101
	ds_write2_b32 v0, v2, v3 offset1:1
	v_pk_mul_f32 v[2:3], v[18:19], v[132:133] op_sel_hi:[1,0]
	v_add_u32_e32 v0, 0x18c0, v101
	ds_write2_b32 v0, v2, v3 offset1:1
	v_pk_mul_f32 v[2:3], v[20:21], v[132:133] op_sel_hi:[1,0]
	v_add_u32_e32 v0, 0x18c8, v101
	ds_write2_b32 v0, v2, v3 offset1:1
	s_waitcnt vmcnt(0)
	v_pk_mul_f32 v[2:3], v[30:31], v[130:131] op_sel_hi:[1,0]
	v_add_u32_e32 v0, 0x1ce0, v101
	ds_write2_b32 v0, v2, v3 offset1:1
	v_pk_mul_f32 v[2:3], v[32:33], v[130:131] op_sel_hi:[1,0]
	v_add_u32_e32 v0, 0x1ce8, v101
	ds_write2_b32 v0, v2, v3 offset1:1
	s_waitcnt lgkmcnt(0)
	ds_read2_b32 v[6:7], v99 offset0:33 offset1:41
	ds_read2_b32 v[8:9], v99 offset1:8
	ds_read2_b32 v[10:11], v99 offset0:66 offset1:74
	ds_read2_b32 v[12:13], v99 offset0:99 offset1:107
	ds_read2_b32 v[14:15], v99 offset0:132 offset1:140
	ds_read2_b32 v[16:17], v99 offset0:165 offset1:173
	ds_read2_b32 v[18:19], v99 offset0:198 offset1:206
	ds_read2_b32 v[20:21], v99 offset0:231 offset1:239
	v_lshl_add_u64 v[22:23], s[14:15], 0, v[116:117]
	v_lshlrev_b32_e32 v0, 1, v106
	s_waitcnt lgkmcnt(6)
	v_cvt_pk_bf16_f32 v2, v8, v6
	s_waitcnt lgkmcnt(4)
	v_cvt_pk_bf16_f32 v3, v10, v12
	s_waitcnt lgkmcnt(2)
	v_cvt_pk_bf16_f32 v4, v14, v16
	s_waitcnt lgkmcnt(0)
	v_cvt_pk_bf16_f32 v5, v18, v20
	v_lshl_add_u64 v[22:23], v[22:23], 0, v[0:1]
	global_store_dwordx4 v[22:23], v[2:5], off sc1 nt
	s_nop 1
	v_cvt_pk_bf16_f32 v2, v9, v7
	v_cvt_pk_bf16_f32 v3, v11, v13
	v_cvt_pk_bf16_f32 v4, v15, v17
	v_cvt_pk_bf16_f32 v5, v19, v21
	ds_read2_b32 v[8:9], v99 offset0:49 offset1:57
	ds_read2_b32 v[10:11], v99 offset0:16 offset1:24
	ds_read2_b32 v[12:13], v99 offset0:82 offset1:90
	ds_read2_b32 v[14:15], v99 offset0:115 offset1:123
	ds_read2_b32 v[16:17], v99 offset0:148 offset1:156
	ds_read2_b32 v[18:19], v99 offset0:181 offset1:189
	ds_read2_b32 v[20:21], v99 offset0:214 offset1:222
	ds_read2_b32 v[22:23], v99 offset0:247 offset1:255
	v_lshl_add_u64 v[6:7], s[14:15], 0, v[114:115]
	v_lshl_add_u64 v[6:7], v[6:7], 0, v[0:1]
	global_store_dwordx4 v[6:7], v[2:5], off sc1 nt
	v_lshl_add_u64 v[6:7], s[14:15], 0, v[112:113]
	v_lshl_add_u64 v[6:7], v[6:7], 0, v[0:1]
	s_waitcnt lgkmcnt(6)
	v_cvt_pk_bf16_f32 v2, v10, v8
	s_waitcnt lgkmcnt(4)
	v_cvt_pk_bf16_f32 v3, v12, v14
	s_waitcnt lgkmcnt(2)
	v_cvt_pk_bf16_f32 v4, v16, v18
	s_waitcnt lgkmcnt(0)
	v_cvt_pk_bf16_f32 v5, v20, v22
	global_store_dwordx4 v[6:7], v[2:5], off sc1 nt
	v_lshl_add_u64 v[6:7], s[14:15], 0, v[110:111]
	v_lshl_add_u64 v[6:7], v[6:7], 0, v[0:1]
	v_cvt_pk_bf16_f32 v2, v11, v9
	v_cvt_pk_bf16_f32 v3, v13, v15
	v_cvt_pk_bf16_f32 v4, v17, v19
	v_cvt_pk_bf16_f32 v5, v21, v23
	global_store_dwordx4 v[6:7], v[2:5], off sc1 nt
	s_waitcnt lgkmcnt(0)
	s_branch .LBB0_199

.LBB0_258:
	s_and_b64 vcc, exec, s[38:39]
	s_cbranch_vccz .LBB0_262
	s_cmp_eq_u32 s31, 0
	s_cbranch_scc1 .LBB0_261
	s_waitcnt vmcnt(6)
	v_pk_mul_f32 v[2:3], v[2:3], v[120:121] op_sel_hi:[1,0]
	ds_write2_b32 v101, v2, v3 offset1:1
	v_pk_mul_f32 v[2:3], v[4:5], v[120:121] op_sel_hi:[1,0]
	ds_write2_b32 v101, v2, v3 offset0:2 offset1:3
	v_pk_mul_f32 v[2:3], v[10:11], v[118:119] op_sel_hi:[1,0]
	v_add_u32_e32 v4, 0x420, v101
	ds_write2_b32 v4, v2, v3 offset1:1
	v_pk_mul_f32 v[2:3], v[12:13], v[118:119] op_sel_hi:[1,0]
	v_add_u32_e32 v4, 0x428, v101
	ds_write2_b32 v4, v2, v3 offset1:1
	v_pk_mul_f32 v[2:3], v[6:7], v[124:125] op_sel_hi:[1,0]
	v_add_u32_e32 v4, 0x840, v101
	ds_write2_b32 v4, v2, v3 offset1:1
	v_pk_mul_f32 v[2:3], v[8:9], v[124:125] op_sel_hi:[1,0]
	v_add_u32_e32 v4, 0x848, v101
	ds_write2_b32 v4, v2, v3 offset1:1
	s_waitcnt vmcnt(5)
	v_pk_mul_f32 v[2:3], v[22:23], v[122:123] op_sel_hi:[1,0]
	v_add_u32_e32 v4, 0xc60, v101
	ds_write2_b32 v4, v2, v3 offset1:1
	v_pk_mul_f32 v[2:3], v[24:25], v[122:123] op_sel_hi:[1,0]
	v_add_u32_e32 v4, 0xc68, v101
	ds_write2_b32 v4, v2, v3 offset1:1
	s_waitcnt vmcnt(4)
	v_pk_mul_f32 v[2:3], v[14:15], v[128:129] op_sel_hi:[1,0]
	v_add_u32_e32 v4, 0x1080, v101
	ds_write2_b32 v4, v2, v3 offset1:1
	v_pk_mul_f32 v[2:3], v[16:17], v[128:129] op_sel_hi:[1,0]
	v_add_u32_e32 v4, 0x1088, v101
	ds_write2_b32 v4, v2, v3 offset1:1
	v_pk_mul_f32 v[2:3], v[26:27], v[126:127] op_sel_hi:[1,0]
	v_add_u32_e32 v4, 0x14a0, v101
	ds_write2_b32 v4, v2, v3 offset1:1
	v_pk_mul_f32 v[2:3], v[28:29], v[126:127] op_sel_hi:[1,0]
	v_add_u32_e32 v4, 0x14a8, v101
	ds_write2_b32 v4, v2, v3 offset1:1
	v_pk_mul_f32 v[2:3], v[18:19], v[132:133] op_sel_hi:[1,0]
	v_add_u32_e32 v4, 0x18c0, v101
	ds_write2_b32 v4, v2, v3 offset1:1
	v_pk_mul_f32 v[2:3], v[20:21], v[132:133] op_sel_hi:[1,0]
	v_add_u32_e32 v4, 0x18c8, v101
	ds_write2_b32 v4, v2, v3 offset1:1
	s_waitcnt vmcnt(0)
	v_pk_mul_f32 v[2:3], v[30:31], v[130:131] op_sel_hi:[1,0]
	v_add_u32_e32 v4, 0x1ce0, v101
	ds_write2_b32 v4, v2, v3 offset1:1
	v_pk_mul_f32 v[2:3], v[32:33], v[130:131] op_sel_hi:[1,0]
	v_add_u32_e32 v4, 0x1ce8, v101
	ds_write2_b32 v4, v2, v3 offset1:1
	s_waitcnt lgkmcnt(0)
	ds_read2_b32 v[6:7], v99 offset0:33 offset1:41
	ds_read2_b32 v[8:9], v99 offset1:8
	ds_read2_b32 v[10:11], v99 offset0:66 offset1:74
	ds_read2_b32 v[12:13], v99 offset0:99 offset1:107
	ds_read2_b32 v[14:15], v99 offset0:132 offset1:140
	ds_read2_b32 v[16:17], v99 offset0:165 offset1:173
	ds_read2_b32 v[18:19], v99 offset0:198 offset1:206
	ds_read2_b32 v[20:21], v99 offset0:231 offset1:239
	v_lshl_add_u64 v[22:23], s[14:15], 0, v[116:117]
	v_lshlrev_b32_e32 v24, 1, v106
	v_mov_b32_e32 v25, v1
	s_waitcnt lgkmcnt(6)
	v_cvt_pk_bf16_f32 v2, v8, v6
	s_waitcnt lgkmcnt(4)
	v_cvt_pk_bf16_f32 v3, v10, v12
	s_waitcnt lgkmcnt(2)
	v_cvt_pk_bf16_f32 v4, v14, v16
	s_waitcnt lgkmcnt(0)
	v_cvt_pk_bf16_f32 v5, v18, v20
	v_lshl_add_u64 v[22:23], v[22:23], 0, v[24:25]
	global_store_dwordx4 v[22:23], v[2:5], off sc1 nt
	s_nop 1
	v_cvt_pk_bf16_f32 v2, v9, v7
	v_cvt_pk_bf16_f32 v3, v11, v13
	v_cvt_pk_bf16_f32 v4, v15, v17
	v_cvt_pk_bf16_f32 v5, v19, v21
	ds_read2_b32 v[8:9], v99 offset0:49 offset1:57
	ds_read2_b32 v[10:11], v99 offset0:16 offset1:24
	ds_read2_b32 v[12:13], v99 offset0:82 offset1:90
	ds_read2_b32 v[14:15], v99 offset0:115 offset1:123
	ds_read2_b32 v[16:17], v99 offset0:148 offset1:156
	ds_read2_b32 v[18:19], v99 offset0:181 offset1:189
	ds_read2_b32 v[20:21], v99 offset0:214 offset1:222
	ds_read2_b32 v[22:23], v99 offset0:247 offset1:255
	v_lshl_add_u64 v[6:7], s[14:15], 0, v[114:115]
	v_lshl_add_u64 v[6:7], v[6:7], 0, v[24:25]
	global_store_dwordx4 v[6:7], v[2:5], off sc1 nt
	v_lshl_add_u64 v[6:7], s[14:15], 0, v[112:113]
	v_lshl_add_u64 v[6:7], v[6:7], 0, v[24:25]
	s_waitcnt lgkmcnt(6)
	v_cvt_pk_bf16_f32 v2, v10, v8
	s_waitcnt lgkmcnt(4)
	v_cvt_pk_bf16_f32 v3, v12, v14
	s_waitcnt lgkmcnt(2)
	v_cvt_pk_bf16_f32 v4, v16, v18
	s_waitcnt lgkmcnt(0)
	v_cvt_pk_bf16_f32 v5, v20, v22
	global_store_dwordx4 v[6:7], v[2:5], off sc1 nt
	v_lshl_add_u64 v[6:7], s[14:15], 0, v[110:111]
	v_lshl_add_u64 v[6:7], v[6:7], 0, v[24:25]
	v_cvt_pk_bf16_f32 v2, v11, v9
	v_cvt_pk_bf16_f32 v3, v13, v15
	v_cvt_pk_bf16_f32 v4, v17, v19
	v_cvt_pk_bf16_f32 v5, v21, v23
	global_store_dwordx4 v[6:7], v[2:5], off sc1 nt
	s_waitcnt lgkmcnt(0)

.LBB0_277:
	s_andn2_b64 vcc, exec, s[38:39]
	s_cbranch_vccnz .LBB0_281
	s_cmp_eq_u32 s31, 0
	s_cbranch_scc1 .LBB0_280
	s_waitcnt vmcnt(0)
	v_pk_mul_f32 v[2:3], v[58:59], v[134:135] op_sel_hi:[1,0]
	ds_write2_b32 v101, v2, v3 offset1:1
	v_pk_mul_f32 v[2:3], v[60:61], v[134:135] op_sel_hi:[1,0]
	ds_write2_b32 v101, v2, v3 offset0:2 offset1:3
	v_pk_mul_f32 v[2:3], v[74:75], v[136:137] op_sel_hi:[1,0]
	v_add_u32_e32 v4, 0x420, v101
	ds_write2_b32 v4, v2, v3 offset1:1
	v_pk_mul_f32 v[2:3], v[76:77], v[136:137] op_sel_hi:[1,0]
	v_add_u32_e32 v4, 0x428, v101
	ds_write2_b32 v4, v2, v3 offset1:1
	v_pk_mul_f32 v[2:3], v[70:71], v[138:139] op_sel_hi:[1,0]
	v_add_u32_e32 v4, 0x840, v101
	ds_write2_b32 v4, v2, v3 offset1:1
	v_pk_mul_f32 v[2:3], v[72:73], v[138:139] op_sel_hi:[1,0]
	v_add_u32_e32 v4, 0x848, v101
	ds_write2_b32 v4, v2, v3 offset1:1
	v_pk_mul_f32 v[2:3], v[82:83], v[140:141] op_sel_hi:[1,0]
	v_add_u32_e32 v4, 0xc60, v101
	ds_write2_b32 v4, v2, v3 offset1:1
	v_pk_mul_f32 v[2:3], v[84:85], v[140:141] op_sel_hi:[1,0]
	v_add_u32_e32 v4, 0xc68, v101
	ds_write2_b32 v4, v2, v3 offset1:1
	v_pk_mul_f32 v[2:3], v[78:79], v[142:143] op_sel_hi:[1,0]
	v_add_u32_e32 v4, 0x1080, v101
	ds_write2_b32 v4, v2, v3 offset1:1
	v_pk_mul_f32 v[2:3], v[80:81], v[142:143] op_sel_hi:[1,0]
	v_add_u32_e32 v4, 0x1088, v101
	ds_write2_b32 v4, v2, v3 offset1:1
	v_pk_mul_f32 v[2:3], v[90:91], v[144:145] op_sel_hi:[1,0]
	v_add_u32_e32 v4, 0x14a0, v101
	ds_write2_b32 v4, v2, v3 offset1:1
	v_pk_mul_f32 v[2:3], v[92:93], v[144:145] op_sel_hi:[1,0]
	v_add_u32_e32 v4, 0x14a8, v101
	ds_write2_b32 v4, v2, v3 offset1:1
	v_pk_mul_f32 v[2:3], v[86:87], v[146:147] op_sel_hi:[1,0]
	v_add_u32_e32 v4, 0x18c0, v101
	ds_write2_b32 v4, v2, v3 offset1:1
	v_pk_mul_f32 v[2:3], v[88:89], v[146:147] op_sel_hi:[1,0]
	v_add_u32_e32 v4, 0x18c8, v101
	ds_write2_b32 v4, v2, v3 offset1:1
	v_pk_mul_f32 v[2:3], v[94:95], v[148:149] op_sel_hi:[1,0]
	v_add_u32_e32 v4, 0x1ce0, v101
	ds_write2_b32 v4, v2, v3 offset1:1
	v_pk_mul_f32 v[2:3], v[96:97], v[148:149] op_sel_hi:[1,0]
	v_add_u32_e32 v4, 0x1ce8, v101
	ds_write2_b32 v4, v2, v3 offset1:1
	s_waitcnt lgkmcnt(0)
	ds_read2_b32 v[6:7], v99 offset0:33 offset1:41
	ds_read2_b32 v[8:9], v99 offset1:8
	ds_read2_b32 v[10:11], v99 offset0:66 offset1:74
	ds_read2_b32 v[12:13], v99 offset0:99 offset1:107
	ds_read2_b32 v[14:15], v99 offset0:132 offset1:140
	ds_read2_b32 v[16:17], v99 offset0:165 offset1:173
	ds_read2_b32 v[18:19], v99 offset0:198 offset1:206
	ds_read2_b32 v[20:21], v99 offset0:231 offset1:239
	v_lshl_add_u64 v[22:23], s[16:17], 0, v[116:117]
	v_lshlrev_b32_e32 v24, 1, v106
	v_mov_b32_e32 v25, v1
	s_waitcnt lgkmcnt(6)
	v_cvt_pk_bf16_f32 v2, v8, v6
	s_waitcnt lgkmcnt(4)
	v_cvt_pk_bf16_f32 v3, v10, v12
	s_waitcnt lgkmcnt(2)
	v_cvt_pk_bf16_f32 v4, v14, v16
	s_waitcnt lgkmcnt(0)
	v_cvt_pk_bf16_f32 v5, v18, v20
	v_lshl_add_u64 v[22:23], v[22:23], 0, v[24:25]
	global_store_dwordx4 v[22:23], v[2:5], off sc1 nt
	s_nop 1
	v_cvt_pk_bf16_f32 v2, v9, v7
	v_cvt_pk_bf16_f32 v3, v11, v13
	v_cvt_pk_bf16_f32 v4, v15, v17
	v_cvt_pk_bf16_f32 v5, v19, v21
	ds_read2_b32 v[8:9], v99 offset0:49 offset1:57
	ds_read2_b32 v[10:11], v99 offset0:16 offset1:24
	ds_read2_b32 v[12:13], v99 offset0:82 offset1:90
	ds_read2_b32 v[14:15], v99 offset0:115 offset1:123
	ds_read2_b32 v[16:17], v99 offset0:148 offset1:156
	ds_read2_b32 v[18:19], v99 offset0:181 offset1:189
	ds_read2_b32 v[20:21], v99 offset0:214 offset1:222
	ds_read2_b32 v[22:23], v99 offset0:247 offset1:255
	v_lshl_add_u64 v[6:7], s[16:17], 0, v[114:115]
	v_lshl_add_u64 v[6:7], v[6:7], 0, v[24:25]
	global_store_dwordx4 v[6:7], v[2:5], off sc1 nt
	v_lshl_add_u64 v[6:7], s[16:17], 0, v[112:113]
	v_lshl_add_u64 v[6:7], v[6:7], 0, v[24:25]
	s_waitcnt lgkmcnt(6)
	v_cvt_pk_bf16_f32 v2, v10, v8
	s_waitcnt lgkmcnt(4)
	v_cvt_pk_bf16_f32 v3, v12, v14
	s_waitcnt lgkmcnt(2)
	v_cvt_pk_bf16_f32 v4, v16, v18
	s_waitcnt lgkmcnt(0)
	v_cvt_pk_bf16_f32 v5, v20, v22
	global_store_dwordx4 v[6:7], v[2:5], off sc1 nt
	v_lshl_add_u64 v[6:7], s[16:17], 0, v[110:111]
	v_lshl_add_u64 v[6:7], v[6:7], 0, v[24:25]
	v_cvt_pk_bf16_f32 v2, v11, v9
	v_cvt_pk_bf16_f32 v3, v13, v15
	v_cvt_pk_bf16_f32 v4, v17, v19
	v_cvt_pk_bf16_f32 v5, v21, v23
	global_store_dwordx4 v[6:7], v[2:5], off sc1 nt
	s_waitcnt lgkmcnt(0)

.LBB0_287:
	s_andn2_b64 vcc, exec, s[36:37]
	s_cbranch_vccnz .LBB0_284
	s_cmp_eq_u32 s31, 0
	s_cbranch_scc1 .LBB0_283
	s_waitcnt vmcnt(6)
	v_pk_mul_f32 v[34:35], v[124:125], v[34:35] op_sel_hi:[0,1]
	ds_write2_b32 v101, v34, v35 offset1:1
	v_pk_mul_f32 v[34:35], v[124:125], v[36:37] op_sel_hi:[0,1]
	ds_write2_b32 v101, v34, v35 offset0:2 offset1:3
	s_waitcnt vmcnt(5)
	v_pk_mul_f32 v[34:35], v[126:127], v[42:43] op_sel_hi:[0,1]
	v_add_u32_e32 v36, 0x420, v101
	ds_write2_b32 v36, v34, v35 offset1:1
	v_pk_mul_f32 v[34:35], v[126:127], v[44:45] op_sel_hi:[0,1]
	v_add_u32_e32 v36, 0x428, v101
	ds_write2_b32 v36, v34, v35 offset1:1
	s_waitcnt vmcnt(4)
	v_pk_mul_f32 v[34:35], v[132:133], v[38:39] op_sel_hi:[0,1]
	v_add_u32_e32 v36, 0x840, v101
	ds_write2_b32 v36, v34, v35 offset1:1
	v_pk_mul_f32 v[34:35], v[132:133], v[40:41] op_sel_hi:[0,1]
	v_add_u32_e32 v36, 0x848, v101
	ds_write2_b32 v36, v34, v35 offset1:1
	v_pk_mul_f32 v[34:35], v[122:123], v[50:51] op_sel_hi:[0,1]
	v_add_u32_e32 v36, 0xc60, v101
	ds_write2_b32 v36, v34, v35 offset1:1
	v_pk_mul_f32 v[34:35], v[122:123], v[52:53] op_sel_hi:[0,1]
	v_add_u32_e32 v36, 0xc68, v101
	ds_write2_b32 v36, v34, v35 offset1:1
	s_waitcnt vmcnt(3)
	v_pk_mul_f32 v[34:35], v[130:131], v[46:47] op_sel_hi:[0,1]
	v_add_u32_e32 v36, 0x1080, v101
	ds_write2_b32 v36, v34, v35 offset1:1
	v_pk_mul_f32 v[34:35], v[130:131], v[48:49] op_sel_hi:[0,1]
	v_add_u32_e32 v36, 0x1088, v101
	ds_write2_b32 v36, v34, v35 offset1:1
	s_waitcnt vmcnt(0)
	v_pk_mul_f32 v[34:35], v[120:121], v[62:63] op_sel_hi:[0,1]
	v_add_u32_e32 v36, 0x14a0, v101
	ds_write2_b32 v36, v34, v35 offset1:1
	v_pk_mul_f32 v[34:35], v[120:121], v[64:65] op_sel_hi:[0,1]
	v_add_u32_e32 v36, 0x14a8, v101
	ds_write2_b32 v36, v34, v35 offset1:1
	v_pk_mul_f32 v[34:35], v[128:129], v[54:55] op_sel_hi:[0,1]
	v_add_u32_e32 v36, 0x18c0, v101
	ds_write2_b32 v36, v34, v35 offset1:1
	v_pk_mul_f32 v[34:35], v[128:129], v[56:57] op_sel_hi:[0,1]
	v_add_u32_e32 v36, 0x18c8, v101
	ds_write2_b32 v36, v34, v35 offset1:1
	v_pk_mul_f32 v[34:35], v[118:119], v[66:67] op_sel_hi:[0,1]
	v_add_u32_e32 v36, 0x1ce0, v101
	ds_write2_b32 v36, v34, v35 offset1:1
	v_pk_mul_f32 v[34:35], v[118:119], v[68:69] op_sel_hi:[0,1]
	v_add_u32_e32 v36, 0x1ce8, v101
	ds_write2_b32 v36, v34, v35 offset1:1
	s_waitcnt lgkmcnt(0)
	ds_read2_b32 v[38:39], v99 offset0:33 offset1:41
	ds_read2_b32 v[40:41], v99 offset1:8
	ds_read2_b32 v[42:43], v99 offset0:66 offset1:74
	ds_read2_b32 v[44:45], v99 offset0:99 offset1:107
	ds_read2_b32 v[46:47], v99 offset0:132 offset1:140
	ds_read2_b32 v[48:49], v99 offset0:165 offset1:173
	ds_read2_b32 v[50:51], v99 offset0:198 offset1:206
	ds_read2_b32 v[52:53], v99 offset0:231 offset1:239
	v_mad_u64_u32 v[54:55], s[36:37], s34, v104, 0
	v_lshl_add_u64 v[54:55], v[54:55], 1, s[14:15]
	v_lshlrev_b32_e32 v56, 1, v106
	v_mov_b32_e32 v57, v1
	s_waitcnt lgkmcnt(6)
	v_cvt_pk_bf16_f32 v34, v40, v38
	s_waitcnt lgkmcnt(4)
	v_cvt_pk_bf16_f32 v35, v42, v44
	s_waitcnt lgkmcnt(2)
	v_cvt_pk_bf16_f32 v36, v46, v48
	s_waitcnt lgkmcnt(0)
	v_cvt_pk_bf16_f32 v37, v50, v52
	v_lshl_add_u64 v[54:55], v[54:55], 0, v[56:57]
	global_store_dwordx4 v[54:55], v[34:37], off sc1 nt
	s_nop 1
	v_cvt_pk_bf16_f32 v34, v41, v39
	v_cvt_pk_bf16_f32 v35, v43, v45
	v_cvt_pk_bf16_f32 v36, v47, v49
	v_cvt_pk_bf16_f32 v37, v51, v53
	v_mad_u64_u32 v[38:39], s[36:37], s34, v102, 0
	ds_read2_b32 v[40:41], v99 offset0:16 offset1:24
	ds_read2_b32 v[42:43], v99 offset0:49 offset1:57
	ds_read2_b32 v[44:45], v99 offset0:82 offset1:90
	ds_read2_b32 v[46:47], v99 offset0:115 offset1:123
	ds_read2_b32 v[48:49], v99 offset0:148 offset1:156
	ds_read2_b32 v[50:51], v99 offset0:181 offset1:189
	ds_read2_b32 v[52:53], v99 offset0:214 offset1:222
	ds_read2_b32 v[54:55], v99 offset0:247 offset1:255
	v_lshl_add_u64 v[38:39], v[38:39], 1, s[14:15]
	v_lshl_add_u64 v[38:39], v[38:39], 0, v[56:57]
	global_store_dwordx4 v[38:39], v[34:37], off sc1 nt
	v_mad_u64_u32 v[38:39], s[36:37], s34, v100, 0
	v_lshl_add_u64 v[38:39], v[38:39], 1, s[14:15]
	s_waitcnt lgkmcnt(6)
	v_cvt_pk_bf16_f32 v34, v40, v42
	s_waitcnt lgkmcnt(4)
	v_cvt_pk_bf16_f32 v35, v44, v46
	s_waitcnt lgkmcnt(2)
	v_cvt_pk_bf16_f32 v36, v48, v50
	s_waitcnt lgkmcnt(0)
	v_cvt_pk_bf16_f32 v37, v52, v54
	v_lshl_add_u64 v[38:39], v[38:39], 0, v[56:57]
	global_store_dwordx4 v[38:39], v[34:37], off sc1 nt
	v_mad_u64_u32 v[38:39], s[36:37], s34, v98, 0
	v_lshl_add_u64 v[38:39], v[38:39], 1, s[14:15]
	v_cvt_pk_bf16_f32 v34, v41, v43
	v_cvt_pk_bf16_f32 v35, v45, v47
	v_cvt_pk_bf16_f32 v36, v49, v51
	v_cvt_pk_bf16_f32 v37, v53, v55
	v_lshl_add_u64 v[38:39], v[38:39], 0, v[56:57]
	global_store_dwordx4 v[38:39], v[34:37], off sc1 nt
	s_waitcnt lgkmcnt(0)
	s_branch .LBB0_283

.LBB0_292:
	s_and_b64 vcc, exec, s[16:17]
	s_cbranch_vccz .LBB0_296
	s_cmp_eq_u32 s31, 0
	s_cbranch_scc1 .LBB0_295
	s_waitcnt vmcnt(6)
	v_pk_mul_f32 v[34:35], v[34:35], v[124:125] op_sel_hi:[1,0]
	ds_write2_b32 v101, v34, v35 offset1:1
	v_pk_mul_f32 v[34:35], v[36:37], v[124:125] op_sel_hi:[1,0]
	ds_write2_b32 v101, v34, v35 offset0:2 offset1:3
	s_waitcnt vmcnt(5)
	v_pk_mul_f32 v[34:35], v[42:43], v[126:127] op_sel_hi:[1,0]
	v_add_u32_e32 v0, 0x420, v101
	ds_write2_b32 v0, v34, v35 offset1:1
	v_pk_mul_f32 v[34:35], v[44:45], v[126:127] op_sel_hi:[1,0]
	v_add_u32_e32 v0, 0x428, v101
	ds_write2_b32 v0, v34, v35 offset1:1
	s_waitcnt vmcnt(4)
	v_pk_mul_f32 v[34:35], v[38:39], v[132:133] op_sel_hi:[1,0]
	v_add_u32_e32 v0, 0x840, v101
	ds_write2_b32 v0, v34, v35 offset1:1
	v_pk_mul_f32 v[34:35], v[40:41], v[132:133] op_sel_hi:[1,0]
	v_add_u32_e32 v0, 0x848, v101
	ds_write2_b32 v0, v34, v35 offset1:1
	v_pk_mul_f32 v[34:35], v[50:51], v[122:123] op_sel_hi:[1,0]
	v_add_u32_e32 v0, 0xc60, v101
	ds_write2_b32 v0, v34, v35 offset1:1
	v_pk_mul_f32 v[34:35], v[52:53], v[122:123] op_sel_hi:[1,0]
	v_add_u32_e32 v0, 0xc68, v101
	ds_write2_b32 v0, v34, v35 offset1:1
	s_waitcnt vmcnt(3)
	v_pk_mul_f32 v[34:35], v[46:47], v[130:131] op_sel_hi:[1,0]
	v_add_u32_e32 v0, 0x1080, v101
	ds_write2_b32 v0, v34, v35 offset1:1
	v_pk_mul_f32 v[34:35], v[48:49], v[130:131] op_sel_hi:[1,0]
	v_add_u32_e32 v0, 0x1088, v101
	ds_write2_b32 v0, v34, v35 offset1:1
	s_waitcnt vmcnt(0)
	v_pk_mul_f32 v[34:35], v[62:63], v[120:121] op_sel_hi:[1,0]
	v_add_u32_e32 v0, 0x14a0, v101
	ds_write2_b32 v0, v34, v35 offset1:1
	v_pk_mul_f32 v[34:35], v[64:65], v[120:121] op_sel_hi:[1,0]
	v_add_u32_e32 v0, 0x14a8, v101
	ds_write2_b32 v0, v34, v35 offset1:1
	v_pk_mul_f32 v[34:35], v[54:55], v[128:129] op_sel_hi:[1,0]
	v_add_u32_e32 v0, 0x18c0, v101
	ds_write2_b32 v0, v34, v35 offset1:1
	v_pk_mul_f32 v[34:35], v[56:57], v[128:129] op_sel_hi:[1,0]
	v_add_u32_e32 v0, 0x18c8, v101
	ds_write2_b32 v0, v34, v35 offset1:1
	v_pk_mul_f32 v[34:35], v[66:67], v[118:119] op_sel_hi:[1,0]
	v_add_u32_e32 v0, 0x1ce0, v101
	ds_write2_b32 v0, v34, v35 offset1:1
	v_pk_mul_f32 v[34:35], v[68:69], v[118:119] op_sel_hi:[1,0]
	v_add_u32_e32 v0, 0x1ce8, v101
	ds_write2_b32 v0, v34, v35 offset1:1
	s_waitcnt lgkmcnt(0)
	ds_read2_b32 v[38:39], v99 offset0:33 offset1:41
	ds_read2_b32 v[40:41], v99 offset1:8
	ds_read2_b32 v[42:43], v99 offset0:66 offset1:74
	ds_read2_b32 v[44:45], v99 offset0:99 offset1:107
	ds_read2_b32 v[46:47], v99 offset0:132 offset1:140
	ds_read2_b32 v[48:49], v99 offset0:165 offset1:173
	ds_read2_b32 v[50:51], v99 offset0:198 offset1:206
	ds_read2_b32 v[52:53], v99 offset0:231 offset1:239
	v_mul_u32_u24_e32 v0, s34, v104
	v_lshlrev_b32_e32 v0, 1, v0
	v_lshl_add_u64 v[54:55], s[14:15], 0, v[0:1]
	v_lshlrev_b32_e32 v0, 1, v106
	s_lshl_b32 s14, s34, 3
	s_waitcnt lgkmcnt(6)
	v_cvt_pk_bf16_f32 v34, v40, v38
	s_waitcnt lgkmcnt(4)
	v_cvt_pk_bf16_f32 v35, v42, v44
	s_waitcnt lgkmcnt(2)
	v_cvt_pk_bf16_f32 v36, v46, v48
	s_waitcnt lgkmcnt(0)
	v_cvt_pk_bf16_f32 v37, v50, v52
	v_lshl_add_u64 v[56:57], v[54:55], 0, v[0:1]
	s_ashr_i32 s15, s14, 31
	global_store_dwordx4 v[56:57], v[34:37], off sc1 nt
	s_lshl_b64 s[14:15], s[14:15], 1
	s_nop 0
	v_cvt_pk_bf16_f32 v34, v41, v39
	v_cvt_pk_bf16_f32 v35, v43, v45
	v_cvt_pk_bf16_f32 v36, v47, v49
	v_cvt_pk_bf16_f32 v37, v51, v53
	v_lshl_add_u64 v[38:39], v[54:55], 0, s[14:15]
	ds_read2_b32 v[42:43], v99 offset0:16 offset1:24
	ds_read2_b32 v[44:45], v99 offset0:49 offset1:57
	ds_read2_b32 v[46:47], v99 offset0:82 offset1:90
	ds_read2_b32 v[48:49], v99 offset0:115 offset1:123
	ds_read2_b32 v[50:51], v99 offset0:148 offset1:156
	ds_read2_b32 v[52:53], v99 offset0:181 offset1:189
	ds_read2_b32 v[54:55], v99 offset0:214 offset1:222
	ds_read2_b32 v[56:57], v99 offset0:247 offset1:255
	v_lshl_add_u64 v[40:41], v[38:39], 0, v[0:1]
	v_lshl_add_u64 v[38:39], v[38:39], 0, s[14:15]
	global_store_dwordx4 v[40:41], v[34:37], off sc1 nt
	v_lshl_add_u64 v[40:41], v[38:39], 0, v[0:1]
	v_lshl_add_u64 v[38:39], v[38:39], 0, s[14:15]
	s_waitcnt lgkmcnt(6)
	v_cvt_pk_bf16_f32 v34, v42, v44
	s_waitcnt lgkmcnt(4)
	v_cvt_pk_bf16_f32 v35, v46, v48
	s_waitcnt lgkmcnt(2)
	v_cvt_pk_bf16_f32 v36, v50, v52
	s_waitcnt lgkmcnt(0)
	v_cvt_pk_bf16_f32 v37, v54, v56
	global_store_dwordx4 v[40:41], v[34:37], off sc1 nt
	v_lshl_add_u64 v[38:39], v[38:39], 0, v[0:1]
	s_nop 0
	v_cvt_pk_bf16_f32 v34, v43, v45
	v_cvt_pk_bf16_f32 v35, v47, v49
	v_cvt_pk_bf16_f32 v36, v51, v53
	v_cvt_pk_bf16_f32 v37, v55, v57
	global_store_dwordx4 v[38:39], v[34:37], off sc1 nt
	s_waitcnt lgkmcnt(0)

.LBB0_314:
	s_andn2_b64 vcc, exec, s[44:45]
	s_cbranch_vccnz .LBB0_318
	s_cmp_eq_u32 s31, 0
	s_cbranch_scc1 .LBB0_317
	s_waitcnt vmcnt(1)
	v_pk_mul_f32 v[26:27], v[126:127], v[26:27] op_sel_hi:[0,1]
	v_add_u32_e32 v0, 0x420, v101
	ds_write2_b32 v0, v26, v27 offset1:1
	v_pk_mul_f32 v[26:27], v[126:127], v[28:29] op_sel_hi:[0,1]
	v_add_u32_e32 v0, 0x428, v101
	ds_write2_b32 v0, v26, v27 offset1:1
	v_pk_mul_f32 v[22:23], v[132:133], v[22:23] op_sel_hi:[0,1]
	v_add_u32_e32 v0, 0x840, v101
	ds_write2_b32 v0, v22, v23 offset1:1
	v_pk_mul_f32 v[22:23], v[132:133], v[24:25] op_sel_hi:[0,1]
	v_add_u32_e32 v0, 0x848, v101
	ds_write2_b32 v0, v22, v23 offset1:1
	v_pk_mul_f32 v[18:19], v[122:123], v[18:19] op_sel_hi:[0,1]
	v_add_u32_e32 v0, 0xc60, v101
	ds_write2_b32 v0, v18, v19 offset1:1
	v_pk_mul_f32 v[18:19], v[122:123], v[20:21] op_sel_hi:[0,1]
	v_add_u32_e32 v0, 0xc68, v101
	ds_write2_b32 v0, v18, v19 offset1:1
	v_pk_mul_f32 v[14:15], v[130:131], v[14:15] op_sel_hi:[0,1]
	v_add_u32_e32 v0, 0x1080, v101
	ds_write2_b32 v0, v14, v15 offset1:1
	v_pk_mul_f32 v[14:15], v[130:131], v[16:17] op_sel_hi:[0,1]
	v_add_u32_e32 v0, 0x1088, v101
	ds_write2_b32 v0, v14, v15 offset1:1
	v_pk_mul_f32 v[10:11], v[120:121], v[10:11] op_sel_hi:[0,1]
	v_add_u32_e32 v0, 0x14a0, v101
	ds_write2_b32 v0, v10, v11 offset1:1
	v_pk_mul_f32 v[10:11], v[120:121], v[12:13] op_sel_hi:[0,1]
	v_add_u32_e32 v0, 0x14a8, v101
	ds_write2_b32 v0, v10, v11 offset1:1
	v_pk_mul_f32 v[6:7], v[128:129], v[6:7] op_sel_hi:[0,1]
	v_add_u32_e32 v0, 0x18c0, v101
	ds_write2_b32 v0, v6, v7 offset1:1
	v_pk_mul_f32 v[6:7], v[128:129], v[8:9] op_sel_hi:[0,1]
	v_add_u32_e32 v0, 0x18c8, v101
	s_waitcnt vmcnt(0)
	v_pk_mul_f32 v[30:31], v[124:125], v[30:31] op_sel_hi:[0,1]
	ds_write2_b32 v0, v6, v7 offset1:1
	v_pk_mul_f32 v[2:3], v[118:119], v[2:3] op_sel_hi:[0,1]
	v_add_u32_e32 v0, 0x1ce0, v101
	ds_write2_b32 v101, v30, v31 offset1:1
	v_pk_mul_f32 v[30:31], v[124:125], v[32:33] op_sel_hi:[0,1]
	ds_write2_b32 v0, v2, v3 offset1:1
	v_pk_mul_f32 v[2:3], v[118:119], v[4:5] op_sel_hi:[0,1]
	v_add_u32_e32 v0, 0x1ce8, v101
	ds_write2_b32 v101, v30, v31 offset0:2 offset1:3
	ds_write2_b32 v0, v2, v3 offset1:1
	s_waitcnt lgkmcnt(0)
	ds_read2_b32 v[6:7], v99 offset0:33 offset1:41
	ds_read2_b32 v[8:9], v99 offset1:8
	ds_read2_b32 v[10:11], v99 offset0:66 offset1:74
	ds_read2_b32 v[12:13], v99 offset0:99 offset1:107
	ds_read2_b32 v[14:15], v99 offset0:132 offset1:140
	ds_read2_b32 v[16:17], v99 offset0:165 offset1:173
	ds_read2_b32 v[18:19], v99 offset0:198 offset1:206
	ds_read2_b32 v[20:21], v99 offset0:231 offset1:239
	v_mad_u64_u32 v[22:23], s[44:45], s34, v104, 0
	v_lshl_add_u64 v[22:23], v[22:23], 1, s[0:1]
	v_lshlrev_b32_e32 v0, 1, v106
	s_waitcnt lgkmcnt(6)
	v_cvt_pk_bf16_f32 v2, v8, v6
	s_waitcnt lgkmcnt(4)
	v_cvt_pk_bf16_f32 v3, v10, v12
	s_waitcnt lgkmcnt(2)
	v_cvt_pk_bf16_f32 v4, v14, v16
	s_waitcnt lgkmcnt(0)
	v_cvt_pk_bf16_f32 v5, v18, v20
	v_lshl_add_u64 v[22:23], v[22:23], 0, v[0:1]
	global_store_dwordx4 v[22:23], v[2:5], off sc1 nt
	s_nop 1
	v_cvt_pk_bf16_f32 v2, v9, v7
	v_cvt_pk_bf16_f32 v3, v11, v13
	v_cvt_pk_bf16_f32 v4, v15, v17
	v_cvt_pk_bf16_f32 v5, v19, v21
	v_mad_u64_u32 v[6:7], s[44:45], s34, v102, 0
	ds_read2_b32 v[8:9], v99 offset0:16 offset1:24
	ds_read2_b32 v[10:11], v99 offset0:49 offset1:57
	ds_read2_b32 v[12:13], v99 offset0:82 offset1:90
	ds_read2_b32 v[14:15], v99 offset0:115 offset1:123
	ds_read2_b32 v[16:17], v99 offset0:148 offset1:156
	ds_read2_b32 v[18:19], v99 offset0:181 offset1:189
	ds_read2_b32 v[20:21], v99 offset0:214 offset1:222
	ds_read2_b32 v[22:23], v99 offset0:247 offset1:255
	v_lshl_add_u64 v[6:7], v[6:7], 1, s[0:1]
	v_lshl_add_u64 v[6:7], v[6:7], 0, v[0:1]
	global_store_dwordx4 v[6:7], v[2:5], off sc1 nt
	v_mad_u64_u32 v[6:7], s[44:45], s34, v100, 0
	v_lshl_add_u64 v[6:7], v[6:7], 1, s[0:1]
	s_waitcnt lgkmcnt(6)
	v_cvt_pk_bf16_f32 v2, v8, v10
	s_waitcnt lgkmcnt(4)
	v_cvt_pk_bf16_f32 v3, v12, v14
	s_waitcnt lgkmcnt(2)
	v_cvt_pk_bf16_f32 v4, v16, v18
	s_waitcnt lgkmcnt(0)
	v_cvt_pk_bf16_f32 v5, v20, v22
	v_lshl_add_u64 v[6:7], v[6:7], 0, v[0:1]
	global_store_dwordx4 v[6:7], v[2:5], off sc1 nt
	v_mad_u64_u32 v[6:7], s[44:45], s34, v98, 0
	v_lshl_add_u64 v[6:7], v[6:7], 1, s[0:1]
	v_cvt_pk_bf16_f32 v2, v9, v11
	v_cvt_pk_bf16_f32 v3, v13, v15
	v_cvt_pk_bf16_f32 v4, v17, v19
	v_cvt_pk_bf16_f32 v5, v21, v23
	v_lshl_add_u64 v[6:7], v[6:7], 0, v[0:1]
	global_store_dwordx4 v[6:7], v[2:5], off sc1 nt
	s_waitcnt lgkmcnt(0)

.LBB0_332:
	s_andn2_b64 vcc, exec, s[44:45]
	s_cbranch_vccnz .LBB0_299
	s_cmp_eq_u32 s31, 0
	s_cbranch_scc1 .LBB0_298
	s_waitcnt vmcnt(1)
	v_pk_mul_f32 v[26:27], v[26:27], v[126:127] op_sel_hi:[1,0]
	v_add_u32_e32 v0, 0x420, v101
	ds_write2_b32 v0, v26, v27 offset1:1
	v_pk_mul_f32 v[26:27], v[28:29], v[126:127] op_sel_hi:[1,0]
	v_add_u32_e32 v0, 0x428, v101
	ds_write2_b32 v0, v26, v27 offset1:1
	v_pk_mul_f32 v[22:23], v[22:23], v[132:133] op_sel_hi:[1,0]
	v_add_u32_e32 v0, 0x840, v101
	ds_write2_b32 v0, v22, v23 offset1:1
	v_pk_mul_f32 v[22:23], v[24:25], v[132:133] op_sel_hi:[1,0]
	v_add_u32_e32 v0, 0x848, v101
	ds_write2_b32 v0, v22, v23 offset1:1
	v_pk_mul_f32 v[18:19], v[18:19], v[122:123] op_sel_hi:[1,0]
	v_add_u32_e32 v0, 0xc60, v101
	ds_write2_b32 v0, v18, v19 offset1:1
	v_pk_mul_f32 v[18:19], v[20:21], v[122:123] op_sel_hi:[1,0]
	v_add_u32_e32 v0, 0xc68, v101
	ds_write2_b32 v0, v18, v19 offset1:1
	v_pk_mul_f32 v[14:15], v[14:15], v[130:131] op_sel_hi:[1,0]
	v_add_u32_e32 v0, 0x1080, v101
	ds_write2_b32 v0, v14, v15 offset1:1
	v_pk_mul_f32 v[14:15], v[16:17], v[130:131] op_sel_hi:[1,0]
	v_add_u32_e32 v0, 0x1088, v101
	ds_write2_b32 v0, v14, v15 offset1:1
	v_pk_mul_f32 v[10:11], v[10:11], v[120:121] op_sel_hi:[1,0]
	v_add_u32_e32 v0, 0x14a0, v101
	ds_write2_b32 v0, v10, v11 offset1:1
	v_pk_mul_f32 v[10:11], v[12:13], v[120:121] op_sel_hi:[1,0]
	v_add_u32_e32 v0, 0x14a8, v101
	ds_write2_b32 v0, v10, v11 offset1:1
	v_pk_mul_f32 v[6:7], v[6:7], v[128:129] op_sel_hi:[1,0]
	v_add_u32_e32 v0, 0x18c0, v101
	ds_write2_b32 v0, v6, v7 offset1:1
	v_pk_mul_f32 v[6:7], v[8:9], v[128:129] op_sel_hi:[1,0]
	v_add_u32_e32 v0, 0x18c8, v101
	s_waitcnt vmcnt(0)
	v_pk_mul_f32 v[30:31], v[30:31], v[124:125] op_sel_hi:[1,0]
	ds_write2_b32 v0, v6, v7 offset1:1
	v_pk_mul_f32 v[2:3], v[2:3], v[118:119] op_sel_hi:[1,0]
	v_add_u32_e32 v0, 0x1ce0, v101
	ds_write2_b32 v101, v30, v31 offset1:1
	v_pk_mul_f32 v[30:31], v[32:33], v[124:125] op_sel_hi:[1,0]
	ds_write2_b32 v0, v2, v3 offset1:1
	v_pk_mul_f32 v[2:3], v[4:5], v[118:119] op_sel_hi:[1,0]
	v_add_u32_e32 v0, 0x1ce8, v101
	ds_write2_b32 v101, v30, v31 offset0:2 offset1:3
	ds_write2_b32 v0, v2, v3 offset1:1
	s_waitcnt lgkmcnt(0)
	ds_read2_b32 v[6:7], v99 offset0:33 offset1:41
	ds_read2_b32 v[8:9], v99 offset1:8
	ds_read2_b32 v[10:11], v99 offset0:66 offset1:74
	ds_read2_b32 v[12:13], v99 offset0:99 offset1:107
	ds_read2_b32 v[14:15], v99 offset0:132 offset1:140
	ds_read2_b32 v[16:17], v99 offset0:165 offset1:173
	ds_read2_b32 v[18:19], v99 offset0:198 offset1:206
	ds_read2_b32 v[20:21], v99 offset0:231 offset1:239
	v_mad_u64_u32 v[22:23], s[36:37], s34, v104, 0
	v_lshl_add_u64 v[22:23], v[22:23], 1, s[0:1]
	v_lshlrev_b32_e32 v0, 1, v106
	s_waitcnt lgkmcnt(6)
	v_cvt_pk_bf16_f32 v2, v8, v6
	s_waitcnt lgkmcnt(4)
	v_cvt_pk_bf16_f32 v3, v10, v12
	s_waitcnt lgkmcnt(2)
	v_cvt_pk_bf16_f32 v4, v14, v16
	s_waitcnt lgkmcnt(0)
	v_cvt_pk_bf16_f32 v5, v18, v20
	v_lshl_add_u64 v[22:23], v[22:23], 0, v[0:1]
	global_store_dwordx4 v[22:23], v[2:5], off sc1 nt
	s_nop 1
	v_cvt_pk_bf16_f32 v2, v9, v7
	v_cvt_pk_bf16_f32 v3, v11, v13
	v_cvt_pk_bf16_f32 v4, v15, v17
	v_cvt_pk_bf16_f32 v5, v19, v21
	v_mad_u64_u32 v[6:7], s[36:37], s34, v102, 0
	ds_read2_b32 v[8:9], v99 offset0:16 offset1:24
	ds_read2_b32 v[10:11], v99 offset0:49 offset1:57
	ds_read2_b32 v[12:13], v99 offset0:82 offset1:90
	ds_read2_b32 v[14:15], v99 offset0:115 offset1:123
	ds_read2_b32 v[16:17], v99 offset0:148 offset1:156
	ds_read2_b32 v[18:19], v99 offset0:181 offset1:189
	ds_read2_b32 v[20:21], v99 offset0:214 offset1:222
	ds_read2_b32 v[22:23], v99 offset0:247 offset1:255
	v_lshl_add_u64 v[6:7], v[6:7], 1, s[0:1]
	v_lshl_add_u64 v[6:7], v[6:7], 0, v[0:1]
	global_store_dwordx4 v[6:7], v[2:5], off sc1 nt
	v_mad_u64_u32 v[6:7], s[36:37], s34, v100, 0
	v_lshl_add_u64 v[6:7], v[6:7], 1, s[0:1]
	s_waitcnt lgkmcnt(6)
	v_cvt_pk_bf16_f32 v2, v8, v10
	s_waitcnt lgkmcnt(4)
	v_cvt_pk_bf16_f32 v3, v12, v14
	s_waitcnt lgkmcnt(2)
	v_cvt_pk_bf16_f32 v4, v16, v18
	s_waitcnt lgkmcnt(0)
	v_cvt_pk_bf16_f32 v5, v20, v22
	v_lshl_add_u64 v[6:7], v[6:7], 0, v[0:1]
	global_store_dwordx4 v[6:7], v[2:5], off sc1 nt
	v_mad_u64_u32 v[6:7], s[36:37], s34, v98, 0
	v_lshl_add_u64 v[6:7], v[6:7], 1, s[0:1]
	v_cvt_pk_bf16_f32 v2, v9, v11
	v_cvt_pk_bf16_f32 v3, v13, v15
	v_cvt_pk_bf16_f32 v4, v17, v19
	v_cvt_pk_bf16_f32 v5, v21, v23
	v_lshl_add_u64 v[6:7], v[6:7], 0, v[0:1]
	global_store_dwordx4 v[6:7], v[2:5], off sc1 nt
	s_waitcnt lgkmcnt(0)
	s_branch .LBB0_298

.LBB0_343:
	s_cmp_eq_u32 s31, 0
	s_cbranch_scc1 .LBB0_345
	s_waitcnt vmcnt(1)
	v_pk_mul_f32 v[26:27], v[26:27], v[126:127] op_sel_hi:[1,0]
	v_add_u32_e32 v0, 0x420, v101
	ds_write2_b32 v0, v26, v27 offset1:1
	v_pk_mul_f32 v[26:27], v[28:29], v[126:127] op_sel_hi:[1,0]
	v_add_u32_e32 v0, 0x428, v101
	ds_write2_b32 v0, v26, v27 offset1:1
	v_pk_mul_f32 v[22:23], v[22:23], v[132:133] op_sel_hi:[1,0]
	v_add_u32_e32 v0, 0x840, v101
	ds_write2_b32 v0, v22, v23 offset1:1
	v_pk_mul_f32 v[22:23], v[24:25], v[132:133] op_sel_hi:[1,0]
	v_add_u32_e32 v0, 0x848, v101
	ds_write2_b32 v0, v22, v23 offset1:1
	v_pk_mul_f32 v[18:19], v[18:19], v[122:123] op_sel_hi:[1,0]
	v_add_u32_e32 v0, 0xc60, v101
	ds_write2_b32 v0, v18, v19 offset1:1
	v_pk_mul_f32 v[18:19], v[20:21], v[122:123] op_sel_hi:[1,0]
	v_add_u32_e32 v0, 0xc68, v101
	ds_write2_b32 v0, v18, v19 offset1:1
	v_pk_mul_f32 v[14:15], v[14:15], v[130:131] op_sel_hi:[1,0]
	v_add_u32_e32 v0, 0x1080, v101
	ds_write2_b32 v0, v14, v15 offset1:1
	v_pk_mul_f32 v[14:15], v[16:17], v[130:131] op_sel_hi:[1,0]
	v_add_u32_e32 v0, 0x1088, v101
	ds_write2_b32 v0, v14, v15 offset1:1
	v_pk_mul_f32 v[10:11], v[10:11], v[120:121] op_sel_hi:[1,0]
	v_add_u32_e32 v0, 0x14a0, v101
	ds_write2_b32 v0, v10, v11 offset1:1
	v_pk_mul_f32 v[10:11], v[12:13], v[120:121] op_sel_hi:[1,0]
	v_add_u32_e32 v0, 0x14a8, v101
	ds_write2_b32 v0, v10, v11 offset1:1
	v_pk_mul_f32 v[6:7], v[6:7], v[128:129] op_sel_hi:[1,0]
	v_add_u32_e32 v0, 0x18c0, v101
	ds_write2_b32 v0, v6, v7 offset1:1
	v_pk_mul_f32 v[6:7], v[8:9], v[128:129] op_sel_hi:[1,0]
	v_add_u32_e32 v0, 0x18c8, v101
	s_waitcnt vmcnt(0)
	v_pk_mul_f32 v[30:31], v[30:31], v[124:125] op_sel_hi:[1,0]
	ds_write2_b32 v0, v6, v7 offset1:1
	v_pk_mul_f32 v[2:3], v[2:3], v[118:119] op_sel_hi:[1,0]
	v_add_u32_e32 v0, 0x1ce0, v101
	ds_write2_b32 v101, v30, v31 offset1:1
	v_pk_mul_f32 v[30:31], v[32:33], v[124:125] op_sel_hi:[1,0]
	ds_write2_b32 v0, v2, v3 offset1:1
	v_pk_mul_f32 v[2:3], v[4:5], v[118:119] op_sel_hi:[1,0]
	v_add_u32_e32 v0, 0x1ce8, v101
	ds_write2_b32 v101, v30, v31 offset0:2 offset1:3
	ds_write2_b32 v0, v2, v3 offset1:1
	s_waitcnt lgkmcnt(0)
	ds_read2_b32 v[6:7], v99 offset0:33 offset1:41
	ds_read2_b32 v[8:9], v99 offset1:8
	ds_read2_b32 v[10:11], v99 offset0:66 offset1:74
	ds_read2_b32 v[12:13], v99 offset0:99 offset1:107
	ds_read2_b32 v[14:15], v99 offset0:132 offset1:140
	ds_read2_b32 v[16:17], v99 offset0:165 offset1:173
	ds_read2_b32 v[18:19], v99 offset0:198 offset1:206
	ds_read2_b32 v[20:21], v99 offset0:231 offset1:239
	v_mad_u64_u32 v[22:23], s[14:15], s34, v104, 0
	v_lshl_add_u64 v[22:23], v[22:23], 1, s[0:1]
	v_lshlrev_b32_e32 v0, 1, v106
	s_waitcnt lgkmcnt(6)
	v_cvt_pk_bf16_f32 v2, v8, v6
	s_waitcnt lgkmcnt(4)
	v_cvt_pk_bf16_f32 v3, v10, v12
	s_waitcnt lgkmcnt(2)
	v_cvt_pk_bf16_f32 v4, v14, v16
	s_waitcnt lgkmcnt(0)
	v_cvt_pk_bf16_f32 v5, v18, v20
	v_lshl_add_u64 v[22:23], v[22:23], 0, v[0:1]
	global_store_dwordx4 v[22:23], v[2:5], off sc1 nt
	s_nop 1
	v_cvt_pk_bf16_f32 v2, v9, v7
	v_cvt_pk_bf16_f32 v3, v11, v13
	v_cvt_pk_bf16_f32 v4, v15, v17
	v_cvt_pk_bf16_f32 v5, v19, v21
	v_mad_u64_u32 v[6:7], s[14:15], s34, v102, 0
	ds_read2_b32 v[8:9], v99 offset0:16 offset1:24
	ds_read2_b32 v[10:11], v99 offset0:49 offset1:57
	ds_read2_b32 v[12:13], v99 offset0:82 offset1:90
	ds_read2_b32 v[14:15], v99 offset0:115 offset1:123
	ds_read2_b32 v[16:17], v99 offset0:148 offset1:156
	ds_read2_b32 v[18:19], v99 offset0:181 offset1:189
	ds_read2_b32 v[20:21], v99 offset0:214 offset1:222
	ds_read2_b32 v[22:23], v99 offset0:247 offset1:255
	v_lshl_add_u64 v[6:7], v[6:7], 1, s[0:1]
	v_lshl_add_u64 v[6:7], v[6:7], 0, v[0:1]
	global_store_dwordx4 v[6:7], v[2:5], off sc1 nt
	v_mad_u64_u32 v[6:7], s[14:15], s34, v100, 0
	v_lshl_add_u64 v[6:7], v[6:7], 1, s[0:1]
	s_waitcnt lgkmcnt(6)
	v_cvt_pk_bf16_f32 v2, v8, v10
	s_waitcnt lgkmcnt(4)
	v_cvt_pk_bf16_f32 v3, v12, v14
	s_waitcnt lgkmcnt(2)
	v_cvt_pk_bf16_f32 v4, v16, v18
	s_waitcnt lgkmcnt(0)
	v_cvt_pk_bf16_f32 v5, v20, v22
	v_lshl_add_u64 v[6:7], v[6:7], 0, v[0:1]
	global_store_dwordx4 v[6:7], v[2:5], off sc1 nt
	v_mad_u64_u32 v[6:7], s[14:15], s34, v98, 0
	v_lshl_add_u64 v[6:7], v[6:7], 1, s[0:1]
	v_cvt_pk_bf16_f32 v2, v9, v11
	v_cvt_pk_bf16_f32 v3, v13, v15
	v_cvt_pk_bf16_f32 v4, v17, v19
	v_cvt_pk_bf16_f32 v5, v21, v23
	v_lshl_add_u64 v[6:7], v[6:7], 0, v[0:1]
	global_store_dwordx4 v[6:7], v[2:5], off sc1 nt
	s_waitcnt lgkmcnt(0)
